# MoE-up GEMM: units of the partial fifth round split between two workgroups by row half (other half's MFMA blocks and stores skipped)
# speedup vs baseline: 1.0256x; 1.0051x over previous
.LBB0_1379:
	v_readlane_b32 s0, v254, 49
	s_add_i32 s38, s38, 1
	v_readlane_b32 s1, v253, 52
	v_mov_b32_e32 v2, s0
	ds_read_b32 v2, v2
	s_mul_i32 s0, s38, s94
	s_add_i32 s0, s1, s0
	s_cmp_eq_u32 s38, 4
	s_cbranch_scc0 .Lt9_map
	s_cmp_eq_u32 s94, 0x100
	s_cbranch_scc0 .Lt9_map
	s_lshr_b32 s0, s1, 1
	s_addk_i32 s0, 0x400
.Lt9_map:
	s_waitcnt lgkmcnt(0)
	v_readfirstlane_b32 s1, v2
	s_lshl_b32 s1, s1, 2
	s_cmp_lt_i32 s0, s1
	s_cselect_b64 s[24:25], -1, 0
	s_cmp_ge_i32 s0, s1
	s_cbranch_scc1 .LBB0_1381
	s_and_b32 s1, s0, -4
	s_add_i32 s16, 0, 0x20000
	s_add_i32 s1, s16, s1
	v_mov_b32_e32 v2, s1
	ds_read_b32 v4, v2 offset:288
	s_ashr_i32 s39, s0, 2
	s_and_b32 s0, s0, 3
	s_waitcnt lgkmcnt(0)
	v_readfirstlane_b32 s1, v4
	s_lshl_b32 s1, s1, 2
	s_add_i32 s16, s16, s1
	v_mov_b32_e32 v2, s16
	ds_read2_b32 v[2:3], v2 offset1:32
	v_lshlrev_b32_e32 v4, 15, v4
	s_or_b32 s16, s1, s0
	s_waitcnt lgkmcnt(0)
	v_sub_u32_e32 v3, s39, v3
	v_lshlrev_b32_e32 v3, 8, v3
	v_sub_u32_e32 v2, v2, v3
	v_add_u32_e32 v156, v3, v4
	v_min_i32_e32 v155, 0x100, v2

.LBB0_1391:
	s_ashr_i32 s17, s16, 31
	s_lshl_b64 s[18:19], s[16:17], 19
	s_add_u32 s18, s3, s18
	s_addc_u32 s19, s28, s19
	s_and_b64 s[24:25], s[24:25], exec
	v_readlane_b32 s24, v253, 44
	s_cselect_b32 s17, s19, s23
	s_cselect_b32 s41, s18, s22
	v_mov_b32_e32 v137, v115
	v_mov_b32_e32 v141, v115
	v_readlane_b32 s25, v253, 45
	s_add_u32 s42, s22, 0x100
	v_mov_b32_e32 v2, 0
	v_lshl_add_u64 v[144:145], s[24:25], 0, v[140:141]
	v_lshl_add_u64 v[146:147], s[24:25], 0, v[136:137]
	s_addc_u32 s43, s23, 0
	s_mov_b32 s44, -2
	s_mov_b64 s[22:23], 0
	v_mov_b32_e32 v3, v2
	v_mov_b32_e32 v4, v2
	v_mov_b32_e32 v5, v2
	v_mov_b32_e32 v6, v2
	v_mov_b32_e32 v7, v2
	v_mov_b32_e32 v8, v2
	v_mov_b32_e32 v9, v2
	v_mov_b32_e32 v18, v2
	v_mov_b32_e32 v19, v2
	v_mov_b32_e32 v20, v2
	v_mov_b32_e32 v21, v2
	v_mov_b32_e32 v22, v2
	v_mov_b32_e32 v23, v2
	v_mov_b32_e32 v24, v2
	v_mov_b32_e32 v25, v2
	v_mov_b32_e32 v34, v2
	v_mov_b32_e32 v35, v2
	v_mov_b32_e32 v36, v2
	v_mov_b32_e32 v37, v2
	v_mov_b32_e32 v38, v2
	v_mov_b32_e32 v39, v2
	v_mov_b32_e32 v40, v2
	v_mov_b32_e32 v41, v2
	v_mov_b32_e32 v50, v2
	v_mov_b32_e32 v51, v2
	v_mov_b32_e32 v52, v2
	v_mov_b32_e32 v53, v2
	v_mov_b32_e32 v54, v2
	v_mov_b32_e32 v55, v2
	v_mov_b32_e32 v56, v2
	v_mov_b32_e32 v57, v2
	v_mov_b32_e32 v10, v2
	v_mov_b32_e32 v11, v2
	v_mov_b32_e32 v12, v2
	v_mov_b32_e32 v13, v2
	v_mov_b32_e32 v14, v2
	v_mov_b32_e32 v15, v2
	v_mov_b32_e32 v16, v2
	v_mov_b32_e32 v17, v2
	v_mov_b32_e32 v26, v2
	v_mov_b32_e32 v27, v2
	v_mov_b32_e32 v28, v2
	v_mov_b32_e32 v29, v2
	v_mov_b32_e32 v30, v2
	v_mov_b32_e32 v31, v2
	v_mov_b32_e32 v32, v2
	v_mov_b32_e32 v33, v2
	v_mov_b32_e32 v42, v2
	v_mov_b32_e32 v43, v2
	v_mov_b32_e32 v44, v2
	v_mov_b32_e32 v45, v2
	v_mov_b32_e32 v46, v2
	v_mov_b32_e32 v47, v2
	v_mov_b32_e32 v48, v2
	v_mov_b32_e32 v49, v2
	v_mov_b32_e32 v58, v2
	v_mov_b32_e32 v59, v2
	v_mov_b32_e32 v60, v2
	v_mov_b32_e32 v61, v2
	v_mov_b32_e32 v62, v2
	v_mov_b32_e32 v63, v2
	v_mov_b32_e32 v64, v2
	v_mov_b32_e32 v65, v2
	v_mov_b32_e32 v66, v2
	v_mov_b32_e32 v67, v2
	v_mov_b32_e32 v68, v2
	v_mov_b32_e32 v69, v2
	v_mov_b32_e32 v70, v2
	v_mov_b32_e32 v71, v2
	v_mov_b32_e32 v72, v2
	v_mov_b32_e32 v73, v2
	v_mov_b32_e32 v82, v2
	v_mov_b32_e32 v83, v2
	v_mov_b32_e32 v84, v2
	v_mov_b32_e32 v85, v2
	v_mov_b32_e32 v86, v2
	v_mov_b32_e32 v87, v2
	v_mov_b32_e32 v88, v2
	v_mov_b32_e32 v89, v2
	v_mov_b32_e32 v98, v2
	v_mov_b32_e32 v99, v2
	v_mov_b32_e32 v100, v2
	v_mov_b32_e32 v101, v2
	v_mov_b32_e32 v102, v2
	v_mov_b32_e32 v103, v2
	v_mov_b32_e32 v104, v2
	v_mov_b32_e32 v105, v2
	v_mov_b32_e32 v116, v2
	v_mov_b32_e32 v117, v2
	v_mov_b32_e32 v118, v2
	v_mov_b32_e32 v119, v2
	v_mov_b32_e32 v120, v2
	v_mov_b32_e32 v121, v2
	v_mov_b32_e32 v122, v2
	v_mov_b32_e32 v123, v2
	v_mov_b32_e32 v74, v2
	v_mov_b32_e32 v75, v2
	v_mov_b32_e32 v76, v2
	v_mov_b32_e32 v77, v2
	v_mov_b32_e32 v78, v2
	v_mov_b32_e32 v79, v2
	v_mov_b32_e32 v80, v2
	v_mov_b32_e32 v81, v2
	v_mov_b32_e32 v90, v2
	v_mov_b32_e32 v91, v2
	v_mov_b32_e32 v92, v2
	v_mov_b32_e32 v93, v2
	v_mov_b32_e32 v94, v2
	v_mov_b32_e32 v95, v2
	v_mov_b32_e32 v96, v2
	v_mov_b32_e32 v97, v2
	v_mov_b32_e32 v106, v2
	v_mov_b32_e32 v107, v2
	v_mov_b32_e32 v108, v2
	v_mov_b32_e32 v109, v2
	v_mov_b32_e32 v110, v2
	v_mov_b32_e32 v111, v2
	v_mov_b32_e32 v112, v2
	v_mov_b32_e32 v113, v2
	v_mov_b32_e32 v124, v2
	v_mov_b32_e32 v125, v2
	v_mov_b32_e32 v126, v2
	v_mov_b32_e32 v127, v2
	v_mov_b32_e32 v128, v2
	v_mov_b32_e32 v129, v2
	v_mov_b32_e32 v130, v2
	v_mov_b32_e32 v131, v2
	s_mov_b32 s36, 0
	s_cmp_eq_u32 s38, 5
	s_cbranch_scc0 .Lt9_flag
	s_cmp_eq_u32 s94, 0x100
	s_cbranch_scc0 .Lt9_flag
	v_readlane_b32 s36, v253, 52
	s_and_b32 s36, s36, 1
	s_xor_b32 s36, s36, 1
	s_add_i32 s36, s36, 1
.Lt9_flag:
.LBB0_1392:
	s_add_u32 s24, s74, s22
	s_addc_u32 s25, s75, s23
	s_add_u32 s26, s24, 0xd851100
	s_addc_u32 s27, s25, 0
	s_add_u32 s45, s42, s22
	s_addc_u32 s46, s43, s23
	s_add_i32 s47, 0, 0x10000
	s_cmpk_eq_i32 s22, 0x700
	s_cselect_b64 vcc, -1, 0
	s_and_b64 s[24:25], vcc, exec
	s_cselect_b32 s27, s59, s27
	s_cselect_b32 s26, s58, s26
	v_add_u32_e32 v161, s47, v154
	s_cselect_b32 s25, s17, s46
	s_cselect_b32 s24, s41, s45
	s_add_i32 s45, 0, 0x14000
	ds_read_b128 v[162:165], v161
	ds_read_b128 v[166:169], v161 offset:1024
	ds_read_b128 v[170:173], v161 offset:2048
	ds_read_b128 v[174:177], v161 offset:3072
	v_add_u32_e32 v161, s45, v154
	ds_read_b128 v[178:181], v161
	ds_read_b128 v[182:185], v161 offset:1024
	ds_read_b128 v[186:189], v161 offset:2048
	ds_read_b128 v[190:193], v161 offset:3072
	v_cndmask_b32_e32 v114, v138, v158, vcc
	v_cndmask_b32_e32 v137, v136, v160, vcc
	v_cndmask_b32_e32 v222, v142, v157, vcc
	v_cndmask_b32_e32 v141, v140, v159, vcc
	v_lshl_add_u64 v[238:239], v[146:147], 0, s[22:23]
	s_add_i32 m0, s21, 0xc000
	ds_read_b128 v[194:197], v143
	ds_read_b128 v[198:201], v143 offset:1024
	ds_read_b128 v[202:205], v143 offset:2048
	ds_read_b128 v[206:209], v143 offset:3072
	ds_read_b128 v[210:213], v143 offset:4096
	ds_read_b128 v[214:217], v143 offset:5120
	ds_read_b128 v[218:221], v143 offset:6144
	ds_read_b128 v[234:237], v143 offset:7168
	global_load_lds_dwordx4 v[238:239], off
	v_lshl_add_u64 v[238:239], v[144:145], 0, s[22:23]
	s_add_i32 m0, s21, 0xe000
	s_nop 0
	global_load_lds_dwordx4 v[238:239], off
	s_waitcnt vmcnt(8)
	s_waitcnt lgkmcnt(0)
	s_barrier
	s_bitcmp1_b32 s36, 0
	s_cbranch_scc1 .Lt9_k0
	s_setprio 1
	s_waitcnt lgkmcnt(0)
	v_mfma_f32_16x16x32_bf16 v[128:131], v[162:165], v[194:197], v[128:131]
	v_mfma_f32_16x16x32_bf16 v[124:127], v[170:173], v[194:197], v[124:127]
	v_mfma_f32_16x16x32_bf16 v[110:113], v[162:165], v[202:205], v[110:113]
	v_mfma_f32_16x16x32_bf16 v[106:109], v[170:173], v[202:205], v[106:109]
	v_mfma_f32_16x16x32_bf16 v[94:97], v[162:165], v[210:213], v[94:97]
	v_mfma_f32_16x16x32_bf16 v[90:93], v[170:173], v[210:213], v[90:93]
	v_mfma_f32_16x16x32_bf16 v[78:81], v[162:165], v[218:221], v[78:81]
	v_mfma_f32_16x16x32_bf16 v[74:77], v[170:173], v[218:221], v[74:77]
	v_mfma_f32_16x16x32_bf16 v[128:131], v[166:169], v[198:201], v[128:131]
	v_mfma_f32_16x16x32_bf16 v[124:127], v[174:177], v[198:201], v[124:127]
	v_mfma_f32_16x16x32_bf16 v[110:113], v[166:169], v[206:209], v[110:113]
	v_mfma_f32_16x16x32_bf16 v[106:109], v[174:177], v[206:209], v[106:109]
	v_mfma_f32_16x16x32_bf16 v[94:97], v[166:169], v[214:217], v[94:97]
	v_mfma_f32_16x16x32_bf16 v[90:93], v[174:177], v[214:217], v[90:93]
	v_mfma_f32_16x16x32_bf16 v[78:81], v[166:169], v[234:237], v[78:81]
	v_mfma_f32_16x16x32_bf16 v[74:77], v[174:177], v[234:237], v[74:77]
	s_setprio 0
	s_setprio 1
	v_mfma_f32_16x16x32_bf16 v[120:123], v[178:181], v[194:197], v[120:123]
	v_mfma_f32_16x16x32_bf16 v[116:119], v[186:189], v[194:197], v[116:119]
	v_mfma_f32_16x16x32_bf16 v[102:105], v[178:181], v[202:205], v[102:105]
	v_mfma_f32_16x16x32_bf16 v[98:101], v[186:189], v[202:205], v[98:101]
	v_mfma_f32_16x16x32_bf16 v[86:89], v[178:181], v[210:213], v[86:89]
	v_mfma_f32_16x16x32_bf16 v[82:85], v[186:189], v[210:213], v[82:85]
	v_mfma_f32_16x16x32_bf16 v[70:73], v[178:181], v[218:221], v[70:73]
	v_mfma_f32_16x16x32_bf16 v[66:69], v[186:189], v[218:221], v[66:69]
	v_mfma_f32_16x16x32_bf16 v[120:123], v[182:185], v[198:201], v[120:123]
	v_mfma_f32_16x16x32_bf16 v[116:119], v[190:193], v[198:201], v[116:119]
	v_mfma_f32_16x16x32_bf16 v[102:105], v[182:185], v[206:209], v[102:105]
	v_mfma_f32_16x16x32_bf16 v[98:101], v[190:193], v[206:209], v[98:101]
	v_mfma_f32_16x16x32_bf16 v[86:89], v[182:185], v[214:217], v[86:89]
	v_mfma_f32_16x16x32_bf16 v[82:85], v[190:193], v[214:217], v[82:85]
	v_mfma_f32_16x16x32_bf16 v[70:73], v[182:185], v[234:237], v[70:73]
	v_mfma_f32_16x16x32_bf16 v[66:69], v[190:193], v[234:237], v[66:69]
	s_setprio 0
.Lt9_k0:
	s_barrier
	s_add_i32 s46, s47, s2
	v_lshl_add_u64 v[238:239], s[24:25], 0, v[132:133]
	s_mov_b32 m0, s46
	ds_read_b128 v[194:197], v143 offset:16384
	ds_read_b128 v[198:201], v143 offset:17408
	ds_read_b128 v[202:205], v143 offset:18432
	ds_read_b128 v[206:209], v143 offset:19456
	ds_read_b128 v[210:213], v143 offset:20480
	ds_read_b128 v[214:217], v143 offset:21504
	ds_read_b128 v[218:221], v143 offset:22528
	ds_read_b128 v[234:237], v143 offset:23552
	global_load_lds_dwordx4 v[238:239], off
	s_add_i32 m0, s46, 0x2000
	s_add_u32 s46, s24, 0x40000
	v_lshl_add_u64 v[240:241], s[24:25], 0, v[134:135]
	s_addc_u32 s47, s25, 0
	s_add_i32 s45, s45, s2
	global_load_lds_dwordx4 v[240:241], off
	v_lshl_add_u64 v[242:243], s[46:47], 0, v[132:133]
	s_mov_b32 m0, s45
	v_mov_b32_e32 v223, v115
	global_load_lds_dwordx4 v[242:243], off
	v_lshl_add_u64 v[242:243], s[46:47], 0, v[134:135]
	s_add_i32 m0, s45, 0x2000
	s_nop 0
	global_load_lds_dwordx4 v[242:243], off
	s_mov_b32 m0, s21
	v_lshl_add_u64 v[242:243], s[26:27], 0, v[114:115]
	global_load_lds_dwordx4 v114, s[26:27]
	s_mov_b32 m0, s29
	s_nop 0
	global_load_lds_dwordx4 v222, s[26:27]
	s_waitcnt vmcnt(8)
	s_waitcnt lgkmcnt(0)
	v_lshl_add_u64 v[222:223], s[26:27], 0, v[222:223]
	s_barrier
	s_bitcmp1_b32 s36, 1
	s_cbranch_scc1 .Lt9_k1
	s_setprio 1
	s_waitcnt lgkmcnt(0)
	v_mfma_f32_16x16x32_bf16 v[62:65], v[162:165], v[194:197], v[62:65]
	v_mfma_f32_16x16x32_bf16 v[58:61], v[170:173], v[194:197], v[58:61]
	v_mfma_f32_16x16x32_bf16 v[46:49], v[162:165], v[202:205], v[46:49]
	v_mfma_f32_16x16x32_bf16 v[42:45], v[170:173], v[202:205], v[42:45]
	v_mfma_f32_16x16x32_bf16 v[30:33], v[162:165], v[210:213], v[30:33]
	v_mfma_f32_16x16x32_bf16 v[26:29], v[170:173], v[210:213], v[26:29]
	v_mfma_f32_16x16x32_bf16 v[14:17], v[162:165], v[218:221], v[14:17]
	v_mfma_f32_16x16x32_bf16 v[10:13], v[170:173], v[218:221], v[10:13]
	v_mfma_f32_16x16x32_bf16 v[62:65], v[166:169], v[198:201], v[62:65]
	v_mfma_f32_16x16x32_bf16 v[58:61], v[174:177], v[198:201], v[58:61]
	v_mfma_f32_16x16x32_bf16 v[46:49], v[166:169], v[206:209], v[46:49]
	v_mfma_f32_16x16x32_bf16 v[42:45], v[174:177], v[206:209], v[42:45]
	v_mfma_f32_16x16x32_bf16 v[30:33], v[166:169], v[214:217], v[30:33]
	v_mfma_f32_16x16x32_bf16 v[26:29], v[174:177], v[214:217], v[26:29]
	v_mfma_f32_16x16x32_bf16 v[14:17], v[166:169], v[234:237], v[14:17]
	v_mfma_f32_16x16x32_bf16 v[10:13], v[174:177], v[234:237], v[10:13]
	s_setprio 0
	s_setprio 1
	v_mfma_f32_16x16x32_bf16 v[54:57], v[178:181], v[194:197], v[54:57]
	v_mfma_f32_16x16x32_bf16 v[50:53], v[186:189], v[194:197], v[50:53]
	v_mfma_f32_16x16x32_bf16 v[38:41], v[178:181], v[202:205], v[38:41]
	v_mfma_f32_16x16x32_bf16 v[34:37], v[186:189], v[202:205], v[34:37]
	v_mfma_f32_16x16x32_bf16 v[22:25], v[178:181], v[210:213], v[22:25]
	v_mfma_f32_16x16x32_bf16 v[18:21], v[186:189], v[210:213], v[18:21]
	v_mfma_f32_16x16x32_bf16 v[6:9], v[178:181], v[218:221], v[6:9]
	v_mfma_f32_16x16x32_bf16 v[2:5], v[186:189], v[218:221], v[2:5]
	v_mfma_f32_16x16x32_bf16 v[54:57], v[182:185], v[198:201], v[54:57]
	v_mfma_f32_16x16x32_bf16 v[50:53], v[190:193], v[198:201], v[50:53]
	v_mfma_f32_16x16x32_bf16 v[38:41], v[182:185], v[206:209], v[38:41]
	v_mfma_f32_16x16x32_bf16 v[34:37], v[190:193], v[206:209], v[34:37]
	v_mfma_f32_16x16x32_bf16 v[22:25], v[182:185], v[214:217], v[22:25]
	v_mfma_f32_16x16x32_bf16 v[18:21], v[190:193], v[214:217], v[18:21]
	v_mfma_f32_16x16x32_bf16 v[6:9], v[182:185], v[234:237], v[6:9]
	v_mfma_f32_16x16x32_bf16 v[2:5], v[190:193], v[234:237], v[2:5]
	s_setprio 0
.Lt9_k1:
	s_barrier
	s_add_i32 s45, 0, 0x18000
	v_add_u32_e32 v114, s45, v154
	s_add_i32 s46, 0, 0x1c000
	ds_read_b128 v[162:165], v114
	ds_read_b128 v[166:169], v114 offset:1024
	ds_read_b128 v[170:173], v114 offset:2048
	ds_read_b128 v[174:177], v114 offset:3072
	v_add_u32_e32 v114, s46, v154
	ds_read_b128 v[178:181], v114
	ds_read_b128 v[182:185], v114 offset:1024
	ds_read_b128 v[186:189], v114 offset:2048
	ds_read_b128 v[190:193], v114 offset:3072
	s_mov_b32 m0, s30
	ds_read_b128 v[194:197], v143 offset:32768
	ds_read_b128 v[198:201], v143 offset:33792
	ds_read_b128 v[202:205], v143 offset:34816
	ds_read_b128 v[206:209], v143 offset:35840
	ds_read_b128 v[210:213], v143 offset:36864
	ds_read_b128 v[214:217], v143 offset:37888
	ds_read_b128 v[218:221], v143 offset:38912
	ds_read_b128 v[234:237], v143 offset:39936
	global_load_lds_dwordx4 v137, s[26:27]
	s_mov_b32 m0, s31
	s_nop 0
	global_load_lds_dwordx4 v141, s[26:27]
	s_waitcnt vmcnt(8)
	s_waitcnt lgkmcnt(0)
	s_barrier
	s_bitcmp1_b32 s36, 0
	s_cbranch_scc1 .Lt9_k2
	s_setprio 1
	s_waitcnt lgkmcnt(0)
	v_mfma_f32_16x16x32_bf16 v[128:131], v[162:165], v[194:197], v[128:131]
	v_mfma_f32_16x16x32_bf16 v[124:127], v[170:173], v[194:197], v[124:127]
	v_mfma_f32_16x16x32_bf16 v[110:113], v[162:165], v[202:205], v[110:113]
	v_mfma_f32_16x16x32_bf16 v[106:109], v[170:173], v[202:205], v[106:109]
	v_mfma_f32_16x16x32_bf16 v[94:97], v[162:165], v[210:213], v[94:97]
	v_mfma_f32_16x16x32_bf16 v[90:93], v[170:173], v[210:213], v[90:93]
	v_mfma_f32_16x16x32_bf16 v[78:81], v[162:165], v[218:221], v[78:81]
	v_mfma_f32_16x16x32_bf16 v[74:77], v[170:173], v[218:221], v[74:77]
	v_mfma_f32_16x16x32_bf16 v[128:131], v[166:169], v[198:201], v[128:131]
	v_mfma_f32_16x16x32_bf16 v[124:127], v[174:177], v[198:201], v[124:127]
	v_mfma_f32_16x16x32_bf16 v[110:113], v[166:169], v[206:209], v[110:113]
	v_mfma_f32_16x16x32_bf16 v[106:109], v[174:177], v[206:209], v[106:109]
	v_mfma_f32_16x16x32_bf16 v[94:97], v[166:169], v[214:217], v[94:97]
	v_mfma_f32_16x16x32_bf16 v[90:93], v[174:177], v[214:217], v[90:93]
	v_mfma_f32_16x16x32_bf16 v[78:81], v[166:169], v[234:237], v[78:81]
	v_mfma_f32_16x16x32_bf16 v[74:77], v[174:177], v[234:237], v[74:77]
	s_setprio 0
	s_setprio 1
	v_mfma_f32_16x16x32_bf16 v[120:123], v[178:181], v[194:197], v[120:123]
	v_mfma_f32_16x16x32_bf16 v[116:119], v[186:189], v[194:197], v[116:119]
	v_mfma_f32_16x16x32_bf16 v[102:105], v[178:181], v[202:205], v[102:105]
	v_mfma_f32_16x16x32_bf16 v[98:101], v[186:189], v[202:205], v[98:101]
	v_mfma_f32_16x16x32_bf16 v[86:89], v[178:181], v[210:213], v[86:89]
	v_mfma_f32_16x16x32_bf16 v[82:85], v[186:189], v[210:213], v[82:85]
	v_mfma_f32_16x16x32_bf16 v[70:73], v[178:181], v[218:221], v[70:73]
	v_mfma_f32_16x16x32_bf16 v[66:69], v[186:189], v[218:221], v[66:69]
	v_mfma_f32_16x16x32_bf16 v[120:123], v[182:185], v[198:201], v[120:123]
	v_mfma_f32_16x16x32_bf16 v[116:119], v[190:193], v[198:201], v[116:119]
	v_mfma_f32_16x16x32_bf16 v[102:105], v[182:185], v[206:209], v[102:105]
	v_mfma_f32_16x16x32_bf16 v[98:101], v[190:193], v[206:209], v[98:101]
	v_mfma_f32_16x16x32_bf16 v[86:89], v[182:185], v[214:217], v[86:89]
	v_mfma_f32_16x16x32_bf16 v[82:85], v[190:193], v[214:217], v[82:85]
	v_mfma_f32_16x16x32_bf16 v[70:73], v[182:185], v[234:237], v[70:73]
	v_mfma_f32_16x16x32_bf16 v[66:69], v[190:193], v[234:237], v[66:69]
	s_setprio 0
.Lt9_k2:
	s_barrier
	s_add_i32 s26, s45, s2
	v_lshl_add_u64 v[238:239], v[238:239], 0, s[78:79]
	s_mov_b32 m0, s26
	ds_read_b128 v[194:197], v143 offset:49152
	ds_read_b128 v[198:201], v143 offset:50176
	ds_read_b128 v[202:205], v143 offset:51200
	ds_read_b128 v[206:209], v143 offset:52224
	ds_read_b128 v[210:213], v143 offset:53248
	ds_read_b128 v[214:217], v143 offset:54272
	ds_read_b128 v[218:221], v143 offset:55296
	ds_read_b128 v[234:237], v143 offset:56320
	global_load_lds_dwordx4 v[238:239], off
	s_add_i32 m0, s26, 0x2000
	s_add_u32 s24, s24, 0x40080
	v_lshl_add_u64 v[238:239], v[240:241], 0, s[78:79]
	s_addc_u32 s25, s25, 0
	s_add_i32 s26, s46, s2
	global_load_lds_dwordx4 v[238:239], off
	v_lshl_add_u64 v[238:239], s[24:25], 0, v[132:133]
	s_mov_b32 m0, s26
	v_lshl_add_u64 v[222:223], v[222:223], 0, s[78:79]
	global_load_lds_dwordx4 v[238:239], off
	v_lshl_add_u64 v[238:239], s[24:25], 0, v[134:135]
	s_add_i32 m0, s26, 0x2000
	s_nop 0
	global_load_lds_dwordx4 v[238:239], off
	v_lshl_add_u64 v[238:239], v[242:243], 0, s[78:79]
	s_mov_b32 m0, s34
	s_nop 0
	global_load_lds_dwordx4 v[238:239], off
	s_mov_b32 m0, s35
	s_nop 0
	global_load_lds_dwordx4 v[222:223], off
	s_waitcnt vmcnt(8)
	s_waitcnt lgkmcnt(0)
	s_barrier
	s_bitcmp1_b32 s36, 1
	s_cbranch_scc1 .Lt9_k3
	s_setprio 1
	s_waitcnt lgkmcnt(0)
	v_mfma_f32_16x16x32_bf16 v[62:65], v[162:165], v[194:197], v[62:65]
	v_mfma_f32_16x16x32_bf16 v[58:61], v[170:173], v[194:197], v[58:61]
	v_mfma_f32_16x16x32_bf16 v[46:49], v[162:165], v[202:205], v[46:49]
	v_mfma_f32_16x16x32_bf16 v[42:45], v[170:173], v[202:205], v[42:45]
	v_mfma_f32_16x16x32_bf16 v[30:33], v[162:165], v[210:213], v[30:33]
	v_mfma_f32_16x16x32_bf16 v[26:29], v[170:173], v[210:213], v[26:29]
	v_mfma_f32_16x16x32_bf16 v[14:17], v[162:165], v[218:221], v[14:17]
	v_mfma_f32_16x16x32_bf16 v[10:13], v[170:173], v[218:221], v[10:13]
	v_mfma_f32_16x16x32_bf16 v[62:65], v[166:169], v[198:201], v[62:65]
	v_mfma_f32_16x16x32_bf16 v[58:61], v[174:177], v[198:201], v[58:61]
	v_mfma_f32_16x16x32_bf16 v[46:49], v[166:169], v[206:209], v[46:49]
	v_mfma_f32_16x16x32_bf16 v[42:45], v[174:177], v[206:209], v[42:45]
	v_mfma_f32_16x16x32_bf16 v[30:33], v[166:169], v[214:217], v[30:33]
	v_mfma_f32_16x16x32_bf16 v[26:29], v[174:177], v[214:217], v[26:29]
	v_mfma_f32_16x16x32_bf16 v[14:17], v[166:169], v[234:237], v[14:17]
	v_mfma_f32_16x16x32_bf16 v[10:13], v[174:177], v[234:237], v[10:13]
	s_setprio 0
	s_setprio 1
	v_mfma_f32_16x16x32_bf16 v[54:57], v[178:181], v[194:197], v[54:57]
	v_mfma_f32_16x16x32_bf16 v[50:53], v[186:189], v[194:197], v[50:53]
	v_mfma_f32_16x16x32_bf16 v[38:41], v[178:181], v[202:205], v[38:41]
	v_mfma_f32_16x16x32_bf16 v[34:37], v[186:189], v[202:205], v[34:37]
	v_mfma_f32_16x16x32_bf16 v[22:25], v[178:181], v[210:213], v[22:25]
	v_mfma_f32_16x16x32_bf16 v[18:21], v[186:189], v[210:213], v[18:21]
	v_mfma_f32_16x16x32_bf16 v[6:9], v[178:181], v[218:221], v[6:9]
	v_mfma_f32_16x16x32_bf16 v[2:5], v[186:189], v[218:221], v[2:5]
	v_mfma_f32_16x16x32_bf16 v[54:57], v[182:185], v[198:201], v[54:57]
	v_mfma_f32_16x16x32_bf16 v[50:53], v[190:193], v[198:201], v[50:53]
	v_mfma_f32_16x16x32_bf16 v[38:41], v[182:185], v[206:209], v[38:41]
	v_mfma_f32_16x16x32_bf16 v[34:37], v[190:193], v[206:209], v[34:37]
	v_mfma_f32_16x16x32_bf16 v[22:25], v[182:185], v[214:217], v[22:25]
	v_mfma_f32_16x16x32_bf16 v[18:21], v[190:193], v[214:217], v[18:21]
	v_mfma_f32_16x16x32_bf16 v[6:9], v[182:185], v[234:237], v[6:9]
	v_mfma_f32_16x16x32_bf16 v[2:5], v[190:193], v[234:237], v[2:5]
	s_setprio 0
.Lt9_k3:
	s_barrier
	s_add_i32 s44, s44, 2
	s_add_u32 s22, s22, 0x100
	s_addc_u32 s23, s23, 0
	s_cmp_gt_u32 s44, 13
	s_cbranch_scc0 .LBB0_1392
	s_and_b64 vcc, exec, s[14:15]
	s_cbranch_vccz .LBB0_1395
	s_barrier
.LBB0_1395:
	v_mul_f32_e32 v114, 0xbfb8aa3b, v128
	v_exp_f32_e32 v114, v114
	v_mul_f32_e32 v137, 0xbfb8aa3b, v129
	v_exp_f32_e32 v137, v137
	v_lshl_add_u32 v136, s40, 8, v153
	v_add_f32_e32 v114, 1.0, v114
	v_rcp_f32_e32 v140, v114
	v_add_f32_e32 v114, 1.0, v137
	v_rcp_f32_e32 v141, v114
	v_ashrrev_i32_e32 v137, 31, v136
	v_mul_f32_e32 v114, 0xbfb8aa3b, v130
	v_lshlrev_b64 v[144:145], 10, v[136:137]
	v_exp_f32_e32 v114, v114
	v_mul_f32_e32 v137, 0xbfb8aa3b, v131
	v_exp_f32_e32 v137, v137
	v_pk_mul_f32 v[128:129], v[128:129], v[140:141]
	v_add_f32_e32 v114, 1.0, v114
	v_pk_mul_f32 v[120:121], v[128:129], v[120:121]
	v_rcp_f32_e32 v128, v114
	v_add_f32_e32 v114, 1.0, v137
	v_rcp_f32_e32 v129, v114
	v_mul_f32_e32 v114, 0xbfb8aa3b, v124
	v_exp_f32_e32 v114, v114
	v_mul_f32_e32 v137, 0xbfb8aa3b, v125
	v_exp_f32_e32 v137, v137
	v_pk_mul_f32 v[128:129], v[130:131], v[128:129]
	v_add_f32_e32 v114, 1.0, v114
	v_mul_f32_e32 v131, 0xbfb8aa3b, v126
	v_rcp_f32_e32 v130, v114
	v_add_f32_e32 v114, 1.0, v137
	v_exp_f32_e32 v137, v131
	v_mul_f32_e32 v131, 0xbfb8aa3b, v127
	v_exp_f32_e32 v141, v131
	v_rcp_f32_e32 v131, v114
	v_add_f32_e32 v114, 1.0, v137
	v_rcp_f32_e32 v140, v114
	v_add_f32_e32 v114, 1.0, v141
	v_rcp_f32_e32 v141, v114
	s_lshl_b32 s17, s20, 7
	s_and_b32 s17, s17, 0x180
	v_readlane_b32 s22, v253, 19
	v_pk_mul_f32 v[124:125], v[124:125], v[130:131]
	v_or_b32_e32 v138, s17, v139
	v_readlane_b32 s23, v253, 20
	v_pk_mul_f32 v[124:125], v[124:125], v[116:117]
	v_pk_mul_f32 v[116:117], v[126:127], v[140:141]
	v_lshl_add_u64 v[144:145], s[22:23], 0, v[144:145]
	v_pk_mul_f32 v[122:123], v[128:129], v[122:123]
	v_pk_mul_f32 v[126:127], v[116:117], v[118:119]
	v_lshlrev_b32_e32 v114, 1, v138
	v_lshl_add_u64 v[116:117], v[144:145], 0, v[114:115]
	v_cvt_pk_bf16_f32 v118, v120, v121
	v_cvt_pk_bf16_f32 v119, v122, v123
	v_cvt_pk_bf16_f32 v120, v124, v125
	v_cvt_pk_bf16_f32 v121, v126, v127
	s_bitcmp1_b32 s36, 0
	s_cbranch_scc1 .Lt9_s0
	global_store_dwordx4 v[116:117], v[118:121], off
.Lt9_s0:
	s_mov_b32 s17, 0x20000
	s_nop 0
	v_mul_f32_e32 v118, 0xbfb8aa3b, v110
	v_exp_f32_e32 v119, v118
	v_mul_f32_e32 v118, 0xbfb8aa3b, v111
	v_exp_f32_e32 v121, v118
	v_or_b32_e32 v118, 16, v136
	v_add_f32_e32 v119, 1.0, v119
	v_rcp_f32_e32 v120, v119
	v_add_f32_e32 v119, 1.0, v121
	v_rcp_f32_e32 v121, v119
	v_ashrrev_i32_e32 v119, 31, v118
	v_lshlrev_b64 v[118:119], 10, v[118:119]
	v_lshl_add_u64 v[118:119], s[22:23], 0, v[118:119]
	v_pk_mul_f32 v[110:111], v[110:111], v[120:121]
	v_mul_f32_e32 v120, 0xbfb8aa3b, v112
	v_mul_f32_e32 v121, 0xbfb8aa3b, v113
	v_exp_f32_e32 v120, v120
	v_exp_f32_e32 v121, v121
	v_pk_mul_f32 v[102:103], v[110:111], v[102:103]
	v_add_f32_e32 v110, 1.0, v120
	v_add_f32_e32 v111, 1.0, v121
	v_mul_f32_e32 v120, 0xbfb8aa3b, v106
	v_mul_f32_e32 v121, 0xbfb8aa3b, v107
	v_rcp_f32_e32 v110, v110
	v_rcp_f32_e32 v111, v111
	v_exp_f32_e32 v120, v120
	v_exp_f32_e32 v121, v121
	v_pk_mul_f32 v[110:111], v[112:113], v[110:111]
	v_add_f32_e32 v112, 1.0, v120
	v_add_f32_e32 v113, 1.0, v121
	v_mul_f32_e32 v120, 0xbfb8aa3b, v108
	v_mul_f32_e32 v121, 0xbfb8aa3b, v109
	v_exp_f32_e32 v120, v120
	v_exp_f32_e32 v121, v121
	v_rcp_f32_e32 v112, v112
	v_rcp_f32_e32 v113, v113
	v_add_f32_e32 v120, 1.0, v120
	v_add_f32_e32 v121, 1.0, v121
	v_rcp_f32_e32 v120, v120
	v_rcp_f32_e32 v121, v121
	v_pk_mul_f32 v[106:107], v[106:107], v[112:113]
	v_pk_mul_f32 v[104:105], v[110:111], v[104:105]
	v_pk_mul_f32 v[106:107], v[106:107], v[98:99]
	v_pk_mul_f32 v[98:99], v[108:109], v[120:121]
	v_lshl_add_u64 v[110:111], v[118:119], 0, v[114:115]
	v_pk_mul_f32 v[108:109], v[98:99], v[100:101]
	v_cvt_pk_bf16_f32 v98, v102, v103
	v_cvt_pk_bf16_f32 v99, v104, v105
	v_cvt_pk_bf16_f32 v100, v106, v107
	v_cvt_pk_bf16_f32 v101, v108, v109
	s_bitcmp1_b32 s36, 0
	s_cbranch_scc1 .Lt9_s1
	global_store_dwordx4 v[110:111], v[98:101], off
.Lt9_s1:
	s_nop 1
	v_mul_f32_e32 v98, 0xbfb8aa3b, v94
	v_exp_f32_e32 v99, v98
	v_mul_f32_e32 v98, 0xbfb8aa3b, v95
	v_exp_f32_e32 v101, v98
	v_or_b32_e32 v98, 32, v136
	v_add_f32_e32 v99, 1.0, v99
	v_rcp_f32_e32 v100, v99
	v_add_f32_e32 v99, 1.0, v101
	v_rcp_f32_e32 v101, v99
	v_ashrrev_i32_e32 v99, 31, v98
	v_lshlrev_b64 v[98:99], 10, v[98:99]
	v_lshl_add_u64 v[98:99], s[22:23], 0, v[98:99]
	v_pk_mul_f32 v[94:95], v[94:95], v[100:101]
	v_mul_f32_e32 v100, 0xbfb8aa3b, v96
	v_mul_f32_e32 v101, 0xbfb8aa3b, v97
	v_exp_f32_e32 v100, v100
	v_exp_f32_e32 v101, v101
	v_pk_mul_f32 v[86:87], v[94:95], v[86:87]
	v_add_f32_e32 v94, 1.0, v100
	v_add_f32_e32 v95, 1.0, v101
	v_mul_f32_e32 v100, 0xbfb8aa3b, v90
	v_mul_f32_e32 v101, 0xbfb8aa3b, v91
	v_rcp_f32_e32 v94, v94
	v_rcp_f32_e32 v95, v95
	v_exp_f32_e32 v100, v100
	v_exp_f32_e32 v101, v101
	v_pk_mul_f32 v[94:95], v[96:97], v[94:95]
	v_add_f32_e32 v96, 1.0, v100
	v_add_f32_e32 v97, 1.0, v101
	v_mul_f32_e32 v100, 0xbfb8aa3b, v92
	v_mul_f32_e32 v101, 0xbfb8aa3b, v93
	v_exp_f32_e32 v100, v100
	v_exp_f32_e32 v101, v101
	v_rcp_f32_e32 v96, v96
	v_rcp_f32_e32 v97, v97
	v_add_f32_e32 v100, 1.0, v100
	v_add_f32_e32 v101, 1.0, v101
	v_rcp_f32_e32 v100, v100
	v_rcp_f32_e32 v101, v101
	v_pk_mul_f32 v[90:91], v[90:91], v[96:97]
	v_pk_mul_f32 v[88:89], v[94:95], v[88:89]
	v_pk_mul_f32 v[90:91], v[90:91], v[82:83]
	v_pk_mul_f32 v[82:83], v[92:93], v[100:101]
	v_lshl_add_u64 v[94:95], v[98:99], 0, v[114:115]
	v_pk_mul_f32 v[92:93], v[82:83], v[84:85]
	v_cvt_pk_bf16_f32 v82, v86, v87
	v_cvt_pk_bf16_f32 v83, v88, v89
	v_cvt_pk_bf16_f32 v84, v90, v91
	v_cvt_pk_bf16_f32 v85, v92, v93
	s_bitcmp1_b32 s36, 0
	s_cbranch_scc1 .Lt9_s2
	global_store_dwordx4 v[94:95], v[82:85], off
.Lt9_s2:
	s_nop 1
	v_mul_f32_e32 v82, 0xbfb8aa3b, v78
	v_exp_f32_e32 v83, v82
	v_mul_f32_e32 v82, 0xbfb8aa3b, v79
	v_exp_f32_e32 v85, v82
	v_or_b32_e32 v82, 48, v136
	v_add_f32_e32 v83, 1.0, v83
	v_rcp_f32_e32 v84, v83
	v_add_f32_e32 v83, 1.0, v85
	v_rcp_f32_e32 v85, v83
	v_ashrrev_i32_e32 v83, 31, v82
	v_lshlrev_b64 v[82:83], 10, v[82:83]
	v_lshl_add_u64 v[82:83], s[22:23], 0, v[82:83]
	v_pk_mul_f32 v[78:79], v[78:79], v[84:85]
	v_mul_f32_e32 v84, 0xbfb8aa3b, v80
	v_mul_f32_e32 v85, 0xbfb8aa3b, v81
	v_exp_f32_e32 v84, v84
	v_exp_f32_e32 v85, v85
	v_pk_mul_f32 v[70:71], v[78:79], v[70:71]
	v_add_f32_e32 v78, 1.0, v84
	v_add_f32_e32 v79, 1.0, v85
	v_mul_f32_e32 v84, 0xbfb8aa3b, v74
	v_mul_f32_e32 v85, 0xbfb8aa3b, v75
	v_rcp_f32_e32 v78, v78
	v_rcp_f32_e32 v79, v79
	v_exp_f32_e32 v84, v84
	v_exp_f32_e32 v85, v85
	v_pk_mul_f32 v[78:79], v[80:81], v[78:79]
	v_add_f32_e32 v80, 1.0, v84
	v_add_f32_e32 v81, 1.0, v85
	v_mul_f32_e32 v84, 0xbfb8aa3b, v76
	v_mul_f32_e32 v85, 0xbfb8aa3b, v77
	v_exp_f32_e32 v84, v84
	v_exp_f32_e32 v85, v85
	v_rcp_f32_e32 v80, v80
	v_rcp_f32_e32 v81, v81
	v_add_f32_e32 v84, 1.0, v84
	v_add_f32_e32 v85, 1.0, v85
	v_rcp_f32_e32 v84, v84
	v_rcp_f32_e32 v85, v85
	v_pk_mul_f32 v[74:75], v[74:75], v[80:81]
	v_pk_mul_f32 v[72:73], v[78:79], v[72:73]
	v_pk_mul_f32 v[74:75], v[74:75], v[66:67]
	v_pk_mul_f32 v[66:67], v[76:77], v[84:85]
	v_lshl_add_u64 v[78:79], v[82:83], 0, v[114:115]
	v_pk_mul_f32 v[76:77], v[66:67], v[68:69]
	v_mul_f32_e32 v67, 0xbfb8aa3b, v62
	v_exp_f32_e32 v68, v67
	v_mul_f32_e32 v67, 0xbfb8aa3b, v63
	v_exp_f32_e32 v69, v67
	v_cvt_pk_bf16_f32 v66, v70, v71
	v_add_f32_e32 v68, 1.0, v68
	v_rcp_f32_e32 v70, v68
	v_add_f32_e32 v68, 1.0, v69
	v_cvt_pk_bf16_f32 v67, v72, v73
	v_rcp_f32_e32 v71, v68
	v_cvt_pk_bf16_f32 v68, v74, v75
	v_cvt_pk_bf16_f32 v69, v76, v77
	s_bitcmp1_b32 s36, 0
	s_cbranch_scc1 .Lt9_s3
	global_store_dwordx4 v[78:79], v[66:69], off
.Lt9_s3:
	v_pk_mul_f32 v[62:63], v[62:63], v[70:71]
	s_nop 0
	v_mul_f32_e32 v66, 0xbfb8aa3b, v64
	v_mul_f32_e32 v67, 0xbfb8aa3b, v65
	v_exp_f32_e32 v66, v66
	v_exp_f32_e32 v67, v67
	v_pk_mul_f32 v[54:55], v[62:63], v[54:55]
	v_add_f32_e32 v62, 1.0, v66
	v_add_f32_e32 v63, 1.0, v67
	v_mul_f32_e32 v66, 0xbfb8aa3b, v58
	v_mul_f32_e32 v67, 0xbfb8aa3b, v59
	v_rcp_f32_e32 v62, v62
	v_rcp_f32_e32 v63, v63
	v_exp_f32_e32 v66, v66
	v_exp_f32_e32 v67, v67
	v_pk_mul_f32 v[62:63], v[64:65], v[62:63]
	v_add_f32_e32 v64, 1.0, v66
	v_add_f32_e32 v65, 1.0, v67
	v_mul_f32_e32 v66, 0xbfb8aa3b, v60
	v_mul_f32_e32 v67, 0xbfb8aa3b, v61
	v_exp_f32_e32 v66, v66
	v_exp_f32_e32 v67, v67
	v_rcp_f32_e32 v64, v64
	v_rcp_f32_e32 v65, v65
	v_add_f32_e32 v66, 1.0, v66
	v_add_f32_e32 v67, 1.0, v67
	v_rcp_f32_e32 v66, v66
	v_rcp_f32_e32 v67, v67
	v_pk_mul_f32 v[58:59], v[58:59], v[64:65]
	v_pk_mul_f32 v[56:57], v[62:63], v[56:57]
	v_pk_mul_f32 v[58:59], v[58:59], v[50:51]
	v_pk_mul_f32 v[50:51], v[60:61], v[66:67]
	s_nop 0
	v_pk_mul_f32 v[60:61], v[50:51], v[52:53]
	v_mul_f32_e32 v53, 0xbfb8aa3b, v46
	v_cvt_pk_bf16_f32 v50, v54, v55
	v_exp_f32_e32 v54, v53
	v_mul_f32_e32 v53, 0xbfb8aa3b, v47
	v_exp_f32_e32 v55, v53
	v_cvt_pk_bf16_f32 v51, v56, v57
	v_add_co_u32_e32 v56, vcc, s17, v116
	v_cvt_pk_bf16_f32 v52, v58, v59
	v_cvt_pk_bf16_f32 v53, v60, v61
	v_add_f32_e32 v54, 1.0, v54
	v_add_f32_e32 v55, 1.0, v55
	v_addc_co_u32_e32 v57, vcc, 0, v117, vcc
	v_rcp_f32_e32 v54, v54
	v_rcp_f32_e32 v55, v55
	s_bitcmp1_b32 s36, 1
	s_cbranch_scc1 .Lt9_s4
	global_store_dwordx4 v[56:57], v[50:53], off
.Lt9_s4:
	s_mov_b32 s17, 0x24000
	v_pk_mul_f32 v[46:47], v[46:47], v[54:55]
	v_mul_f32_e32 v50, 0xbfb8aa3b, v48
	v_mul_f32_e32 v51, 0xbfb8aa3b, v49
	v_exp_f32_e32 v50, v50
	v_exp_f32_e32 v51, v51
	v_pk_mul_f32 v[38:39], v[46:47], v[38:39]
	v_add_f32_e32 v46, 1.0, v50
	v_add_f32_e32 v47, 1.0, v51
	v_mul_f32_e32 v50, 0xbfb8aa3b, v42
	v_mul_f32_e32 v51, 0xbfb8aa3b, v43
	v_rcp_f32_e32 v46, v46
	v_rcp_f32_e32 v47, v47
	v_exp_f32_e32 v50, v50
	v_exp_f32_e32 v51, v51
	v_pk_mul_f32 v[46:47], v[48:49], v[46:47]
	v_add_f32_e32 v48, 1.0, v50
	v_add_f32_e32 v49, 1.0, v51
	v_mul_f32_e32 v50, 0xbfb8aa3b, v44
	v_mul_f32_e32 v51, 0xbfb8aa3b, v45
	v_exp_f32_e32 v50, v50
	v_exp_f32_e32 v51, v51
	v_rcp_f32_e32 v48, v48
	v_rcp_f32_e32 v49, v49
	v_add_f32_e32 v50, 1.0, v50
	v_add_f32_e32 v51, 1.0, v51
	v_rcp_f32_e32 v50, v50
	v_rcp_f32_e32 v51, v51
	v_pk_mul_f32 v[42:43], v[42:43], v[48:49]
	v_pk_mul_f32 v[40:41], v[46:47], v[40:41]
	v_pk_mul_f32 v[42:43], v[42:43], v[34:35]
	v_pk_mul_f32 v[34:35], v[44:45], v[50:51]
	s_nop 0
	v_pk_mul_f32 v[44:45], v[34:35], v[36:37]
	v_mul_f32_e32 v37, 0xbfb8aa3b, v30
	v_cvt_pk_bf16_f32 v34, v38, v39
	v_exp_f32_e32 v38, v37
	v_mul_f32_e32 v37, 0xbfb8aa3b, v31
	v_exp_f32_e32 v39, v37
	v_cvt_pk_bf16_f32 v35, v40, v41
	v_add_co_u32_e32 v40, vcc, s17, v116
	v_cvt_pk_bf16_f32 v36, v42, v43
	v_cvt_pk_bf16_f32 v37, v44, v45
	v_add_f32_e32 v38, 1.0, v38
	v_add_f32_e32 v39, 1.0, v39
	v_addc_co_u32_e32 v41, vcc, 0, v117, vcc
	v_rcp_f32_e32 v38, v38
	v_rcp_f32_e32 v39, v39
	s_bitcmp1_b32 s36, 1
	s_cbranch_scc1 .Lt9_s5
	global_store_dwordx4 v[40:41], v[34:37], off
.Lt9_s5:
	s_mov_b32 s17, 0x28000
	v_pk_mul_f32 v[30:31], v[30:31], v[38:39]
	v_mul_f32_e32 v34, 0xbfb8aa3b, v32
	v_mul_f32_e32 v35, 0xbfb8aa3b, v33
	v_exp_f32_e32 v34, v34
	v_exp_f32_e32 v35, v35
	v_pk_mul_f32 v[22:23], v[30:31], v[22:23]
	v_add_f32_e32 v30, 1.0, v34
	v_add_f32_e32 v31, 1.0, v35
	v_mul_f32_e32 v34, 0xbfb8aa3b, v26
	v_mul_f32_e32 v35, 0xbfb8aa3b, v27
	v_rcp_f32_e32 v30, v30
	v_rcp_f32_e32 v31, v31
	v_exp_f32_e32 v34, v34
	v_exp_f32_e32 v35, v35
	v_pk_mul_f32 v[30:31], v[32:33], v[30:31]
	v_add_f32_e32 v32, 1.0, v34
	v_add_f32_e32 v33, 1.0, v35
	v_mul_f32_e32 v34, 0xbfb8aa3b, v28
	v_mul_f32_e32 v35, 0xbfb8aa3b, v29
	v_exp_f32_e32 v34, v34
	v_exp_f32_e32 v35, v35
	v_rcp_f32_e32 v32, v32
	v_rcp_f32_e32 v33, v33
	v_add_f32_e32 v34, 1.0, v34
	v_add_f32_e32 v35, 1.0, v35
	v_rcp_f32_e32 v34, v34
	v_rcp_f32_e32 v35, v35
	v_pk_mul_f32 v[26:27], v[26:27], v[32:33]
	v_pk_mul_f32 v[24:25], v[30:31], v[24:25]
	v_pk_mul_f32 v[26:27], v[26:27], v[18:19]
	v_pk_mul_f32 v[18:19], v[28:29], v[34:35]
	s_nop 0
	v_pk_mul_f32 v[28:29], v[18:19], v[20:21]
	v_mul_f32_e32 v21, 0xbfb8aa3b, v14
	v_cvt_pk_bf16_f32 v18, v22, v23
	v_exp_f32_e32 v22, v21
	v_mul_f32_e32 v21, 0xbfb8aa3b, v15
	v_exp_f32_e32 v23, v21
	v_cvt_pk_bf16_f32 v19, v24, v25
	v_add_co_u32_e32 v24, vcc, s17, v116
	v_cvt_pk_bf16_f32 v20, v26, v27
	v_cvt_pk_bf16_f32 v21, v28, v29
	v_add_f32_e32 v22, 1.0, v22
	v_add_f32_e32 v23, 1.0, v23
	v_addc_co_u32_e32 v25, vcc, 0, v117, vcc
	v_rcp_f32_e32 v22, v22
	v_rcp_f32_e32 v23, v23
	s_bitcmp1_b32 s36, 1
	s_cbranch_scc1 .Lt9_s6
	global_store_dwordx4 v[24:25], v[18:21], off
.Lt9_s6:
	v_pk_mul_f32 v[14:15], v[14:15], v[22:23]
	s_nop 0
	v_mul_f32_e32 v18, 0xbfb8aa3b, v16
	v_mul_f32_e32 v19, 0xbfb8aa3b, v17
	v_exp_f32_e32 v18, v18
	v_exp_f32_e32 v19, v19
	v_pk_mul_f32 v[6:7], v[14:15], v[6:7]
	v_add_f32_e32 v14, 1.0, v18
	v_add_f32_e32 v15, 1.0, v19
	v_mul_f32_e32 v18, 0xbfb8aa3b, v10
	v_mul_f32_e32 v19, 0xbfb8aa3b, v11
	v_rcp_f32_e32 v14, v14
	v_rcp_f32_e32 v15, v15
	v_exp_f32_e32 v18, v18
	v_exp_f32_e32 v19, v19
	v_pk_mul_f32 v[14:15], v[16:17], v[14:15]
	v_add_f32_e32 v16, 1.0, v18
	v_add_f32_e32 v17, 1.0, v19
	v_mul_f32_e32 v18, 0xbfb8aa3b, v12
	v_mul_f32_e32 v19, 0xbfb8aa3b, v13
	v_exp_f32_e32 v18, v18
	v_exp_f32_e32 v19, v19
	v_rcp_f32_e32 v16, v16
	v_rcp_f32_e32 v17, v17
	v_add_f32_e32 v18, 1.0, v18
	v_add_f32_e32 v19, 1.0, v19
	v_rcp_f32_e32 v18, v18
	v_rcp_f32_e32 v19, v19
	v_pk_mul_f32 v[10:11], v[10:11], v[16:17]
	v_pk_mul_f32 v[8:9], v[14:15], v[8:9]
	v_pk_mul_f32 v[10:11], v[10:11], v[2:3]
	v_pk_mul_f32 v[2:3], v[12:13], v[18:19]
	s_nop 0
	v_pk_mul_f32 v[12:13], v[2:3], v[4:5]
	v_cvt_pk_bf16_f32 v2, v6, v7
	v_add_co_u32_e32 v6, vcc, 0x2c000, v116
	v_cvt_pk_bf16_f32 v3, v8, v9
	s_nop 0
	v_addc_co_u32_e32 v7, vcc, 0, v117, vcc
	v_cvt_pk_bf16_f32 v4, v10, v11
	v_cvt_pk_bf16_f32 v5, v12, v13
	s_and_b64 vcc, exec, s[0:1]
	s_mov_b64 s[0:1], -1
	s_bitcmp1_b32 s36, 1
	s_cbranch_scc1 .Lt9_s7
	global_store_dwordx4 v[6:7], v[2:5], off
.Lt9_s7:
	s_cbranch_vccnz .LBB0_1378
	s_andn2_b64 vcc, exec, s[12:13]
	s_cbranch_vccnz .LBB0_1377
	s_barrier
	s_branch .LBB0_1377
